# strategy 1 (wait placement) in P7 norm loop: next group's pos loads issued before this group's x1b stores, counted waits skip the stores
# speedup vs baseline: 1.0077x; 1.0008x over previous
.LBB0_1137:
	s_add_i32 s16, s63, s62
	s_lshl_b32 s17, s16, 12
	s_or_b32 s22, s16, 1
	s_and_b32 s17, s17, 0x3e000
	s_add_u32 s18, s33, s17
	s_addc_u32 s19, s53, 0
	s_ashr_i32 s20, s16, 6
	v_mov_b32_e32 v209, v206
	s_ashr_i32 s21, s20, 31
	s_lshl_b64 s[20:21], s[20:21], 12
	v_lshlrev_b32_e32 v142, 2, v209
	s_add_u32 s20, s33, s20
	v_ashrrev_i32_e32 v143, 31, v142
	s_addc_u32 s21, s53, s21
	v_lshlrev_b64 v[170:171], 2, v[142:143]
	v_lshl_add_u64 v[70:71], s[20:21], 0, v[170:171]
	s_waitcnt lgkmcnt(0)
	global_load_dwordx4 v[66:69], v[70:71], off
	s_lshl_b32 s17, s22, 12
	s_and_b32 s17, s17, 0x3f000
	s_add_u32 s20, s33, s17
	s_addc_u32 s21, s53, 0
	s_ashr_i32 s17, s16, 31
	s_lshl_b64 s[24:25], s[16:17], 12
	s_add_u32 s24, s60, s24
	s_addc_u32 s25, s61, s25
	s_ashr_i32 s23, s22, 31
	s_lshl_b64 s[22:23], s[22:23], 12
	s_add_u32 s22, s60, s22
	v_lshlrev_b64 v[122:123], 1, v[142:143]
	s_addc_u32 s23, s61, s23
	s_waitcnt vmcnt(24)
	v_lshlrev_b32_e32 v72, 16, v74
	v_and_b32_e32 v73, 0xffff0000, v74
	v_lshlrev_b32_e32 v116, 16, v75
	v_and_b32_e32 v117, 0xffff0000, v75
	s_waitcnt vmcnt(20)
	v_lshlrev_b32_e32 v118, 16, v82
	v_and_b32_e32 v119, 0xffff0000, v82
	v_lshl_add_u64 v[166:167], s[24:25], 0, v[122:123]
	v_lshl_add_u64 v[168:169], s[22:23], 0, v[122:123]
	v_lshlrev_b32_e32 v120, 16, v83
	v_and_b32_e32 v121, 0xffff0000, v83
	s_mov_b64 s[22:23], 0x1000
	v_and_b32_e32 v180, 64, v202
	v_xor_b32_e32 v181, 1, v202
	v_add_u32_e32 v238, 64, v180
	v_readlane_b32 s76, v252, 9
	v_lshl_add_u64 v[212:213], v[170:171], 0, s[50:51]
	v_readlane_b32 s90, v252, 23
	v_readlane_b32 s91, v252, 24
	v_lshl_add_u64 v[184:185], s[42:43], 0, v[170:171]
	s_waitcnt vmcnt(2)
	v_lshlrev_b32_e32 v190, 16, v108
	v_lshl_add_u64 v[188:189], s[90:91], 0, v[170:171]
	v_and_b32_e32 v191, 0xffff0000, v108
	v_lshlrev_b32_e32 v192, 16, v109
	v_and_b32_e32 v193, 0xffff0000, v109
	v_lshlrev_b32_e32 v178, 16, v103
	v_and_b32_e32 v179, 0xffff0000, v103
	s_waitcnt vmcnt(1)
	v_lshlrev_b32_e32 v182, 16, v110
	v_and_b32_e32 v183, 0xffff0000, v110
	v_lshlrev_b32_e32 v186, 16, v111
	v_and_b32_e32 v187, 0xffff0000, v111
	v_xor_b32_e32 v207, 2, v202
	v_xor_b32_e32 v236, 4, v202
	v_xor_b32_e32 v211, 8, v202
	v_xor_b32_e32 v210, 16, v202
	v_xor_b32_e32 v237, 32, v202
	s_lshl_b64 s[16:17], s[16:17], 11
	v_lshl_add_u32 v209, v209, 3, 0
	s_add_i32 s73, s63, s65
	v_readlane_b32 s77, v252, 10
	v_readlane_b32 s78, v252, 11
	v_readlane_b32 s79, v252, 12
	v_readlane_b32 s80, v252, 13
	v_readlane_b32 s81, v252, 14
	v_readlane_b32 s82, v252, 15
	v_readlane_b32 s83, v252, 16
	v_readlane_b32 s84, v252, 17
	v_readlane_b32 s85, v252, 18
	v_readlane_b32 s86, v252, 19
	v_readlane_b32 s87, v252, 20
	v_readlane_b32 s88, v252, 21
	v_readlane_b32 s89, v252, 22
	s_waitcnt vmcnt(0)
	v_pk_add_f32 v[122:123], v[4:5], v[68:69]
	v_pk_add_f32 v[124:125], v[2:3], v[66:67]
	v_pk_add_f32 v[66:67], v[10:11], v[66:67]
	v_pk_add_f32 v[68:69], v[12:13], v[68:69]
	v_pk_add_f32 v[158:159], v[122:123], v[116:117]
	v_pk_add_f32 v[162:163], v[124:125], v[72:73]
	v_pk_add_f32 v[164:165], v[66:67], v[118:119]
	v_cvt_pk_bf16_f32 v248, v162, v163
	v_cvt_pk_bf16_f32 v249, v158, v159
	v_pk_add_f32 v[160:161], v[68:69], v[120:121]
	v_cvt_pk_bf16_f32 v250, v164, v165
	v_lshlrev_b32_e32 v72, 16, v76
	v_cvt_pk_bf16_f32 v251, v160, v161
	global_load_dwordx4 v[66:69], v[70:71], off offset:1024
	global_store_dwordx2 v[166:167], v[248:249], off
	global_store_dwordx2 v[168:169], v[250:251], off
	v_and_b32_e32 v73, 0xffff0000, v76
	v_lshlrev_b32_e32 v116, 16, v77
	v_and_b32_e32 v117, 0xffff0000, v77
	v_lshlrev_b32_e32 v118, 16, v84
	v_and_b32_e32 v119, 0xffff0000, v84
	v_lshlrev_b32_e32 v120, 16, v85
	v_and_b32_e32 v121, 0xffff0000, v85
	v_mov_b32_e32 v216, v163
	v_mov_b32_e32 v220, v159
	v_mov_b32_e32 v224, v165
	v_mov_b32_e32 v228, v161
	v_mov_b32_e32 v214, v162
	v_mov_b32_e32 v218, v158
	v_mov_b32_e32 v222, v164
	v_mov_b32_e32 v226, v160
	s_waitcnt vmcnt(2)
	v_pk_add_f32 v[122:123], v[8:9], v[68:69]
	v_pk_add_f32 v[124:125], v[6:7], v[66:67]
	v_pk_add_f32 v[66:67], v[14:15], v[66:67]
	v_pk_add_f32 v[68:69], v[16:17], v[68:69]
	v_pk_add_f32 v[150:151], v[122:123], v[116:117]
	v_pk_add_f32 v[152:153], v[124:125], v[72:73]
	v_pk_add_f32 v[156:157], v[66:67], v[118:119]
	v_cvt_pk_bf16_f32 v248, v152, v153
	v_cvt_pk_bf16_f32 v249, v150, v151
	v_pk_add_f32 v[154:155], v[68:69], v[120:121]
	v_cvt_pk_bf16_f32 v250, v156, v157
	v_lshlrev_b32_e32 v72, 16, v78
	v_cvt_pk_bf16_f32 v251, v154, v155
	global_load_dwordx4 v[66:69], v[70:71], off offset:2048
	global_store_dwordx2 v[166:167], v[248:249], off offset:512
	global_store_dwordx2 v[168:169], v[250:251], off offset:512
	v_and_b32_e32 v73, 0xffff0000, v78
	v_lshlrev_b32_e32 v116, 16, v79
	v_and_b32_e32 v117, 0xffff0000, v79
	v_lshlrev_b32_e32 v118, 16, v88
	v_and_b32_e32 v119, 0xffff0000, v88
	v_lshlrev_b32_e32 v120, 16, v89
	v_and_b32_e32 v121, 0xffff0000, v89
	v_mov_b32_e32 v217, v153
	v_mov_b32_e32 v221, v151
	v_mov_b32_e32 v225, v157
	v_mov_b32_e32 v229, v155
	v_mov_b32_e32 v215, v152
	v_mov_b32_e32 v219, v150
	v_mov_b32_e32 v223, v156
	v_mov_b32_e32 v227, v154
	s_waitcnt vmcnt(2)
	v_pk_add_f32 v[122:123], v[20:21], v[68:69]
	v_pk_add_f32 v[124:125], v[18:19], v[66:67]
	v_pk_add_f32 v[66:67], v[26:27], v[66:67]
	v_pk_add_f32 v[68:69], v[28:29], v[68:69]
	v_pk_add_f32 v[140:141], v[122:123], v[116:117]
	v_pk_add_f32 v[144:145], v[124:125], v[72:73]
	v_pk_add_f32 v[148:149], v[66:67], v[118:119]
	v_cvt_pk_bf16_f32 v248, v144, v145
	v_cvt_pk_bf16_f32 v249, v140, v141
	v_pk_add_f32 v[146:147], v[68:69], v[120:121]
	v_cvt_pk_bf16_f32 v250, v148, v149
	v_lshl_add_u64 v[120:121], v[170:171], 0, s[22:23]
	v_cvt_pk_bf16_f32 v251, v146, v147
	global_load_dwordx4 v[66:69], v[70:71], off offset:3072
	global_store_dwordx2 v[166:167], v[248:249], off offset:1024
	global_store_dwordx2 v[168:169], v[250:251], off offset:1024
	v_lshl_add_u64 v[122:123], s[18:19], 0, v[120:121]
	v_lshlrev_b32_e32 v70, 16, v80
	v_and_b32_e32 v71, 0xffff0000, v80
	v_lshlrev_b32_e32 v72, 16, v81
	v_and_b32_e32 v73, 0xffff0000, v81
	v_lshlrev_b32_e32 v116, 16, v90
	v_and_b32_e32 v117, 0xffff0000, v90
	v_add_co_u32_e32 v122, vcc, s66, v122
	v_lshlrev_b32_e32 v118, 16, v91
	v_and_b32_e32 v119, 0xffff0000, v91
	v_addc_co_u32_e32 v123, vcc, 0, v123, vcc
	v_lshl_add_u64 v[120:121], s[20:21], 0, v[120:121]
	s_waitcnt vmcnt(2)
	v_pk_add_f32 v[124:125], v[24:25], v[68:69]
	v_pk_add_f32 v[126:127], v[22:23], v[66:67]
	v_pk_add_f32 v[66:67], v[30:31], v[66:67]
	v_pk_add_f32 v[68:69], v[32:33], v[68:69]
	v_pk_add_f32 v[132:133], v[124:125], v[72:73]
	v_pk_add_f32 v[136:137], v[126:127], v[70:71]
	v_pk_add_f32 v[138:139], v[66:67], v[116:117]
	v_cvt_pk_bf16_f32 v248, v136, v137
	v_cvt_pk_bf16_f32 v249, v132, v133
	v_pk_add_f32 v[134:135], v[68:69], v[118:119]
	v_cvt_pk_bf16_f32 v250, v138, v139
	v_add_co_u32_e32 v70, vcc, s66, v120
	v_cvt_pk_bf16_f32 v251, v134, v135
	global_load_dwordx4 v[66:69], v[122:123], off
	v_addc_co_u32_e32 v71, vcc, 0, v121, vcc
	global_load_dwordx4 v[70:73], v[70:71], off
	global_store_dwordx2 v[166:167], v[248:249], off offset:1536
	global_store_dwordx2 v[168:169], v[250:251], off offset:1536
	v_lshl_add_u64 v[124:125], v[170:171], 0, s[46:47]
	v_lshl_add_u64 v[126:127], s[18:19], 0, v[124:125]
	v_lshlrev_b32_e32 v116, 16, v94
	v_and_b32_e32 v117, 0xffff0000, v94
	v_lshlrev_b32_e32 v118, 16, v95
	v_and_b32_e32 v119, 0xffff0000, v95
	v_add_co_u32_e32 v172, vcc, s66, v126
	v_lshlrev_b32_e32 v120, 16, v104
	v_and_b32_e32 v121, 0xffff0000, v104
	v_lshlrev_b32_e32 v122, 16, v105
	v_and_b32_e32 v123, 0xffff0000, v105
	v_addc_co_u32_e32 v173, vcc, 0, v127, vcc
	v_lshl_add_u64 v[174:175], s[20:21], 0, v[124:125]
	s_waitcnt vmcnt(3)
	v_pk_add_f32 v[68:69], v[36:37], v[68:69]
	v_pk_add_f32 v[66:67], v[34:35], v[66:67]
	v_pk_add_f32 v[124:125], v[68:69], v[118:119]
	s_waitcnt vmcnt(2)
	v_pk_add_f32 v[72:73], v[40:41], v[72:73]
	v_pk_add_f32 v[70:71], v[38:39], v[70:71]
	v_pk_add_f32 v[128:129], v[66:67], v[116:117]
	v_pk_add_f32 v[126:127], v[72:73], v[122:123]
	v_cvt_pk_bf16_f32 v248, v128, v129
	v_cvt_pk_bf16_f32 v249, v124, v125
	v_pk_add_f32 v[130:131], v[70:71], v[120:121]
	v_add_co_u32_e32 v70, vcc, s66, v174
	v_cvt_pk_bf16_f32 v250, v130, v131
	v_cvt_pk_bf16_f32 v251, v126, v127
	global_load_dwordx4 v[66:69], v[172:173], off
	v_addc_co_u32_e32 v71, vcc, 0, v175, vcc
	global_load_dwordx4 v[70:73], v[70:71], off
	global_store_dwordx2 v[166:167], v[248:249], off offset:2048
	global_store_dwordx2 v[168:169], v[250:251], off offset:2048
	v_lshl_add_u64 v[120:121], v[170:171], 0, s[48:49]
	v_lshl_add_u64 v[174:175], s[18:19], 0, v[120:121]
	v_lshlrev_b32_e32 v118, 16, v96
	v_and_b32_e32 v119, 0xffff0000, v96
	v_lshlrev_b32_e32 v116, 16, v97
	v_and_b32_e32 v117, 0xffff0000, v97
	v_add_co_u32_e32 v174, vcc, s66, v174
	v_lshlrev_b32_e32 v122, 16, v106
	v_and_b32_e32 v123, 0xffff0000, v106
	v_lshlrev_b32_e32 v172, 16, v107
	v_and_b32_e32 v173, 0xffff0000, v107
	v_addc_co_u32_e32 v175, vcc, 0, v175, vcc
	v_lshl_add_u64 v[176:177], s[20:21], 0, v[120:121]
	s_waitcnt vmcnt(3)
	v_pk_add_f32 v[68:69], v[44:45], v[68:69]
	v_pk_add_f32 v[66:67], v[42:43], v[66:67]
	v_pk_add_f32 v[116:117], v[68:69], v[116:117]
	s_waitcnt vmcnt(2)
	v_pk_add_f32 v[72:73], v[48:49], v[72:73]
	v_pk_add_f32 v[70:71], v[46:47], v[70:71]
	v_pk_add_f32 v[120:121], v[66:67], v[118:119]
	v_pk_add_f32 v[118:119], v[72:73], v[172:173]
	v_cvt_pk_bf16_f32 v248, v120, v121
	v_cvt_pk_bf16_f32 v249, v116, v117
	v_pk_add_f32 v[122:123], v[70:71], v[122:123]
	v_add_co_u32_e32 v70, vcc, s66, v176
	v_cvt_pk_bf16_f32 v250, v122, v123
	v_cvt_pk_bf16_f32 v251, v118, v119
	global_load_dwordx4 v[66:69], v[174:175], off
	v_addc_co_u32_e32 v71, vcc, 0, v177, vcc
	global_load_dwordx4 v[70:73], v[70:71], off
	global_store_dwordx2 v[166:167], v[248:249], off offset:2560
	global_store_dwordx2 v[168:169], v[250:251], off offset:2560
	v_cmp_lt_i32_e32 vcc, v181, v238
	v_lshlrev_b32_e32 v174, 16, v98
	v_and_b32_e32 v175, 0xffff0000, v98
	v_cndmask_b32_e32 v180, v202, v181, vcc
	v_lshlrev_b32_e32 v208, 2, v180
	v_lshl_add_u64 v[180:181], s[44:45], 0, v[170:171]
	v_lshl_add_u64 v[170:171], s[18:19], 0, v[212:213]
	v_lshlrev_b32_e32 v176, 16, v99
	v_and_b32_e32 v177, 0xffff0000, v99
	v_add_co_u32_e32 v170, vcc, s66, v170
	v_lshl_add_u64 v[212:213], s[20:21], 0, v[212:213]
	s_nop 0
	v_addc_co_u32_e32 v171, vcc, 0, v171, vcc
	v_add_co_u32_e32 v212, vcc, s66, v212
	v_lshlrev_b32_e32 v172, 16, v102
	s_nop 0
	v_addc_co_u32_e32 v213, vcc, 0, v213, vcc
	v_and_b32_e32 v173, 0xffff0000, v102
	v_cmp_lt_i32_e32 vcc, v207, v238
	s_mul_i32 s18, s97, 0x2020
	s_waitcnt vmcnt(3)
	v_pk_add_f32 v[68:69], v[52:53], v[68:69]
	v_pk_add_f32 v[66:67], v[50:51], v[66:67]
	s_waitcnt vmcnt(2)
	v_pk_add_f32 v[72:73], v[56:57], v[72:73]
	v_pk_add_f32 v[230:231], v[54:55], v[70:71]
	v_pk_add_f32 v[70:71], v[68:69], v[176:177]
	v_pk_add_f32 v[174:175], v[66:67], v[174:175]
	v_pk_add_f32 v[72:73], v[72:73], v[192:193]
	v_cvt_pk_bf16_f32 v66, v174, v175
	v_cvt_pk_bf16_f32 v67, v70, v71
	v_pk_add_f32 v[176:177], v[230:231], v[190:191]
	s_nop 0
	v_cvt_pk_bf16_f32 v68, v176, v177
	v_cvt_pk_bf16_f32 v69, v72, v73
	global_store_dwordx2 v[166:167], v[66:67], off offset:3072
	global_store_dwordx2 v[168:169], v[68:69], off offset:3072
	global_load_dwordx4 v[66:69], v[170:171], off
	s_nop 0
	global_load_dwordx4 v[190:193], v[212:213], off
	v_pk_mul_f32 v[170:171], v[216:217], v[216:217]
	v_pk_mul_f32 v[212:213], v[220:221], v[220:221]
	v_pk_mul_f32 v[216:217], v[224:225], v[224:225]
	v_pk_mul_f32 v[220:221], v[228:229], v[228:229]
	v_pk_fma_f32 v[170:171], v[214:215], v[214:215], v[170:171]
	v_pk_fma_f32 v[212:213], v[218:219], v[218:219], v[212:213]
	v_pk_fma_f32 v[214:215], v[222:223], v[222:223], v[216:217]
	v_pk_fma_f32 v[216:217], v[226:227], v[226:227], v[220:221]
	v_pk_add_f32 v[170:171], v[170:171], v[212:213]
	v_pk_add_f32 v[212:213], v[214:215], v[216:217]
	v_pk_mul_f32 v[214:215], v[140:141], v[140:141]
	v_pk_mul_f32 v[216:217], v[144:145], v[144:145]
	v_pk_mul_f32 v[218:219], v[146:147], v[146:147]
	v_pk_mul_f32 v[220:221], v[148:149], v[148:149]
	v_pk_mov_b32 v[222:223], v[216:217], v[214:215] op_sel:[1,0]
	v_mov_b32_e32 v217, v215
	v_pk_mov_b32 v[214:215], v[220:221], v[218:219] op_sel:[1,0]
	v_mov_b32_e32 v221, v219
	v_pk_add_f32 v[216:217], v[222:223], v[216:217]
	v_mul_f32_e32 v222, v139, v139
	v_mul_f32_e32 v224, v135, v135
	v_pk_add_f32 v[214:215], v[214:215], v[220:221]
	v_mul_f32_e32 v218, v137, v137
	v_mul_f32_e32 v220, v133, v133
	v_pk_fma_f32 v[222:223], v[138:139], v[138:139], v[222:223] op_sel_hi:[1,1,0]
	v_pk_fma_f32 v[224:225], v[134:135], v[134:135], v[224:225] op_sel_hi:[1,1,0]
	v_pk_add_f32 v[170:171], v[170:171], v[170:171] op_sel:[0,1] op_sel_hi:[1,0]
	v_pk_add_f32 v[212:213], v[212:213], v[212:213] op_sel:[0,1] op_sel_hi:[1,0]
	v_pk_add_f32 v[216:217], v[216:217], v[216:217] op_sel:[0,1] op_sel_hi:[1,0]
	v_pk_add_f32 v[214:215], v[214:215], v[214:215] op_sel:[0,1] op_sel_hi:[1,0]
	v_pk_fma_f32 v[218:219], v[136:137], v[136:137], v[218:219] op_sel_hi:[1,1,0]
	v_pk_fma_f32 v[220:221], v[132:133], v[132:133], v[220:221] op_sel_hi:[1,1,0]
	v_mul_f32_e32 v223, v130, v130
	v_mul_f32_e32 v225, v131, v131
	v_mul_f32_e32 v226, v126, v126
	v_mul_f32_e32 v227, v127, v127
	v_mul_f32_e32 v171, v128, v128
	v_mul_f32_e32 v217, v129, v129
	v_mul_f32_e32 v219, v124, v124
	v_mul_f32_e32 v221, v125, v125
	v_mov_b32_e32 v213, v223
	v_mov_b32_e32 v215, v225
	v_mov_b32_e32 v223, v226
	v_mov_b32_e32 v225, v227
	v_pk_add_f32 v[170:171], v[170:171], v[216:217]
	v_pk_add_f32 v[216:217], v[218:219], v[220:221]
	v_pk_add_f32 v[212:213], v[212:213], v[214:215]
	v_pk_add_f32 v[214:215], v[222:223], v[224:225]
	v_pk_add_f32 v[170:171], v[170:171], v[216:217]
	v_pk_add_f32 v[212:213], v[212:213], v[214:215]
	v_pk_add_f32 v[220:221], v[170:171], v[170:171] op_sel:[0,1] op_sel_hi:[1,0]
	v_pk_add_f32 v[222:223], v[212:213], v[212:213] op_sel:[0,1] op_sel_hi:[1,0]
	v_pk_mul_f32 v[170:171], v[116:117], v[116:117]
	v_pk_mul_f32 v[212:213], v[120:121], v[120:121]
	v_pk_mul_f32 v[214:215], v[118:119], v[118:119]
	v_pk_mul_f32 v[216:217], v[122:123], v[122:123]
	v_pk_mov_b32 v[218:219], v[212:213], v[170:171] op_sel:[1,0]
	v_mov_b32_e32 v213, v171
	v_pk_mov_b32 v[170:171], v[216:217], v[214:215] op_sel:[1,0]
	v_mov_b32_e32 v217, v215
	v_pk_add_f32 v[170:171], v[170:171], v[216:217]
	v_pk_add_f32 v[212:213], v[218:219], v[212:213]
	v_pk_add_f32 v[226:227], v[170:171], v[170:171] op_sel:[0,1] op_sel_hi:[1,0]
	v_mul_f32_e32 v170, v175, v175
	v_pk_fma_f32 v[228:229], v[174:175], v[174:175], v[170:171] op_sel_hi:[1,1,0]
	v_pk_add_f32 v[224:225], v[212:213], v[212:213] op_sel:[0,1] op_sel_hi:[1,0]
	v_mul_f32_e32 v212, v71, v71
	v_mul_f32_e32 v214, v177, v177
	v_mul_f32_e32 v216, v73, v73
	v_pk_fma_f32 v[230:231], v[70:71], v[70:71], v[212:213] op_sel_hi:[1,1,0]
	v_pk_fma_f32 v[232:233], v[176:177], v[176:177], v[214:215] op_sel_hi:[1,1,0]
	v_pk_fma_f32 v[234:235], v[72:73], v[72:73], v[216:217] op_sel_hi:[1,1,0]
	s_waitcnt vmcnt(1)
	v_pk_add_f32 v[68:69], v[60:61], v[68:69]
	v_pk_add_f32 v[170:171], v[58:59], v[66:67]
	s_waitcnt vmcnt(0)
	v_pk_add_f32 v[192:193], v[64:65], v[192:193]
	v_pk_add_f32 v[190:191], v[62:63], v[190:191]
	v_pk_add_f32 v[66:67], v[68:69], v[178:179]
	v_pk_add_f32 v[170:171], v[170:171], v[172:173]
	v_pk_add_f32 v[68:69], v[192:193], v[186:187]
	v_cvt_pk_bf16_f32 v178, v170, v171
	v_cvt_pk_bf16_f32 v179, v66, v67
	v_pk_add_f32 v[172:173], v[190:191], v[182:183]
	v_mul_f32_e32 v221, v170, v170
	v_cvt_pk_bf16_f32 v182, v172, v173
	v_cvt_pk_bf16_f32 v183, v68, v69
	global_store_dwordx2 v[166:167], v[178:179], off offset:3584
	global_store_dwordx2 v[168:169], v[182:183], off offset:3584
	global_load_dwordx4 v[190:193], v[184:185], off
	global_load_dwordx4 v[212:215], v[188:189], off
	global_load_dwordx4 v[216:219], v[180:181], off
	v_mul_f32_e32 v225, v171, v171
	v_mul_f32_e32 v229, v66, v66
	v_mul_f32_e32 v231, v67, v67
	v_mul_f32_e32 v223, v172, v172
	v_mul_f32_e32 v227, v173, v173
	v_mul_f32_e32 v233, v68, v68
	v_mul_f32_e32 v235, v69, v69
	v_pk_add_f32 v[166:167], v[220:221], v[224:225]
	v_pk_add_f32 v[168:169], v[228:229], v[230:231]
	v_pk_add_f32 v[178:179], v[222:223], v[226:227]
	v_pk_add_f32 v[182:183], v[232:233], v[234:235]
	v_pk_add_f32 v[166:167], v[166:167], v[168:169]
	v_pk_add_f32 v[168:169], v[178:179], v[182:183]
	v_mov_b32_e32 v179, v166
	v_mov_b32_e32 v178, v168
	v_mov_b32_e32 v166, v169
	v_pk_add_f32 v[166:167], v[178:179], v[166:167]
	ds_bpermute_b32 v179, v208, v167
	ds_bpermute_b32 v178, v208, v166
	v_cndmask_b32_e32 v168, v202, v207, vcc
	v_lshlrev_b32_e32 v169, 2, v168
	v_cmp_lt_i32_e32 vcc, v236, v238
	v_lshl_add_u64 v[220:221], s[34:35], 0, v[142:143]
	s_waitcnt lgkmcnt(0)
	v_pk_add_f32 v[166:167], v[166:167], v[178:179]
	ds_bpermute_b32 v183, v169, v167
	ds_bpermute_b32 v182, v169, v166
	v_cndmask_b32_e32 v168, v202, v236, vcc
	v_lshlrev_b32_e32 v179, 2, v168
	v_cmp_lt_i32_e32 vcc, v211, v238
	v_lshl_add_u64 v[142:143], v[220:221], 0, s[16:17]
	s_waitcnt lgkmcnt(0)
	v_pk_add_f32 v[166:167], v[166:167], v[182:183]
	ds_bpermute_b32 v187, v179, v167
	ds_bpermute_b32 v186, v179, v166
	v_cndmask_b32_e32 v168, v202, v211, vcc
	v_lshlrev_b32_e32 v182, 2, v168
	v_cmp_lt_i32_e32 vcc, v210, v238
	v_mov_b32_e32 v222, 0
	s_waitcnt lgkmcnt(0)
	v_pk_add_f32 v[166:167], v[166:167], v[186:187]
	ds_bpermute_b32 v187, v182, v167
	ds_bpermute_b32 v186, v182, v166
	v_cndmask_b32_e32 v168, v202, v210, vcc
	v_lshlrev_b32_e32 v183, 2, v168
	v_cmp_lt_i32_e32 vcc, v237, v238
	v_mov_b32_e32 v207, 0
	s_waitcnt lgkmcnt(0)
	v_pk_add_f32 v[166:167], v[166:167], v[186:187]
	ds_bpermute_b32 v211, v183, v167
	ds_bpermute_b32 v210, v183, v166
	v_cndmask_b32_e32 v178, v202, v237, vcc
	v_lshlrev_b32_e32 v186, 2, v178
	v_add_u32_e32 v187, s18, v209
	s_add_i32 s18, s63, s64
	s_waitcnt lgkmcnt(0)
	v_pk_add_f32 v[166:167], v[166:167], v[210:211]
	ds_bpermute_b32 v211, v186, v167
	ds_bpermute_b32 v210, v186, v166
	s_ashr_i32 s19, s18, 31
	s_lshl_b64 s[18:19], s[18:19], 11
	s_cmpk_gt_i32 s73, 0x3fff
	s_cselect_b64 s[56:57], -1, 0
	s_waitcnt lgkmcnt(0)
	v_pk_add_f32 v[166:167], v[166:167], v[210:211]
	s_waitcnt vmcnt(2)
	v_pk_add_f32 v[190:191], v[190:191], 1.0 op_sel_hi:[1,0]
	v_pk_fma_f32 v[166:167], v[166:167], s[52:53], v[114:115] op_sel_hi:[1,0,0]
	s_waitcnt vmcnt(1)
	v_pk_mul_f32 v[190:191], v[212:213], v[190:191]
	v_mul_f32_e32 v168, 0x4b800000, v167
	v_cmp_gt_f32_e32 vcc, s67, v167
	v_mul_f32_e32 v178, 0x4b800000, v166
	v_cmp_gt_f32_e64 s[16:17], s67, v166
	v_cndmask_b32_e32 v167, v167, v168, vcc
	v_rsq_f32_e32 v168, v167
	v_cndmask_b32_e64 v166, v166, v178, s[16:17]
	v_rsq_f32_e32 v210, v166
	v_pk_add_f32 v[192:193], v[192:193], 1.0 op_sel_hi:[1,0]
	v_mul_f32_e32 v178, 0x45800000, v168
	v_cndmask_b32_e32 v178, v168, v178, vcc
	v_mul_f32_e32 v211, 0x45800000, v210
	v_cndmask_b32_e64 v168, v210, v211, s[16:17]
	v_pk_mul_f32 v[162:163], v[162:163], v[178:179] op_sel_hi:[1,0]
	v_pk_mul_f32 v[164:165], v[164:165], v[168:169] op_sel_hi:[1,0]
	s_waitcnt vmcnt(0)
	v_pk_fma_f32 v[162:163], v[190:191], v[162:163], v[216:217]
	v_pk_mul_f32 v[158:159], v[158:159], v[178:179] op_sel_hi:[1,0]
	v_pk_mul_f32 v[160:161], v[160:161], v[168:169] op_sel_hi:[1,0]
	v_pk_mul_f32 v[192:193], v[214:215], v[192:193]
	v_pk_fma_f32 v[164:165], v[190:191], v[164:165], v[216:217]
	v_cvt_pk_bf16_f32 v190, v162, v163
	v_med3_f32 v162, v162, s68, v203
	v_med3_f32 v163, v163, s68, v203
	v_pk_fma_f32 v[158:159], v[192:193], v[158:159], v[218:219]
	v_pk_fma_f32 v[160:161], v[192:193], v[160:161], v[218:219]
	v_med3_f32 v192, v164, s68, v203
	v_cvt_pk_fp8_f32 v222, v162, v163
	v_med3_f32 v162, v165, s68, v203
	v_cvt_pk_fp8_f32 v207, v192, v162
	v_cvt_pk_bf16_f32 v191, v158, v159
	v_med3_f32 v158, v158, s68, v203
	v_med3_f32 v159, v159, s68, v203
	v_med3_f32 v163, v160, s68, v203
	v_cvt_pk_fp8_f32 v222, v158, v159 op_sel:[0,0,1]
	v_med3_f32 v158, v161, s68, v203
	v_cvt_pk_fp8_f32 v207, v163, v158 op_sel:[0,0,1]
	v_lshl_add_u64 v[166:167], v[220:221], 0, s[18:19]
	ds_write_b64 v187, v[190:191]
	global_store_dword v[142:143], v222, off
	v_cvt_pk_bf16_f32 v164, v164, v165
	v_cvt_pk_bf16_f32 v165, v160, v161
	global_store_dword v[166:167], v207, off
	global_load_dwordx4 v[160:163], v[184:185], off offset:1024
	global_load_dwordx4 v[190:193], v[188:189], off offset:1024
	global_load_dwordx4 v[210:213], v[180:181], off offset:1024
	s_mul_i32 s16, s64, 0x1010
	v_pk_mul_f32 v[152:153], v[152:153], v[178:179] op_sel_hi:[1,0]
	v_add_u32_e32 v158, s16, v209
	v_pk_mul_f32 v[156:157], v[156:157], v[168:169] op_sel_hi:[1,0]
	v_mov_b32_e32 v159, 0
	v_pk_mul_f32 v[150:151], v[150:151], v[178:179] op_sel_hi:[1,0]
	v_pk_mul_f32 v[154:155], v[154:155], v[168:169] op_sel_hi:[1,0]
	ds_write_b64 v158, v[164:165]
	v_mov_b32_e32 v207, 0
	v_pk_mul_f32 v[144:145], v[144:145], v[178:179] op_sel_hi:[1,0]
	v_pk_mul_f32 v[148:149], v[148:149], v[168:169] op_sel_hi:[1,0]
	v_pk_mul_f32 v[140:141], v[140:141], v[178:179] op_sel_hi:[1,0]
	v_pk_mul_f32 v[146:147], v[146:147], v[168:169] op_sel_hi:[1,0]
	v_pk_mul_f32 v[136:137], v[136:137], v[178:179] op_sel_hi:[1,0]
	v_pk_mul_f32 v[138:139], v[138:139], v[168:169] op_sel_hi:[1,0]
	v_pk_mul_f32 v[132:133], v[132:133], v[178:179] op_sel_hi:[1,0]
	v_pk_mul_f32 v[134:135], v[134:135], v[168:169] op_sel_hi:[1,0]
	v_pk_mul_f32 v[128:129], v[128:129], v[178:179] op_sel_hi:[1,0]
	v_pk_mul_f32 v[130:131], v[130:131], v[168:169] op_sel_hi:[1,0]
	v_pk_mul_f32 v[124:125], v[124:125], v[178:179] op_sel_hi:[1,0]
	v_pk_mul_f32 v[126:127], v[126:127], v[168:169] op_sel_hi:[1,0]
	v_pk_mul_f32 v[120:121], v[120:121], v[178:179] op_sel_hi:[1,0]
	v_pk_mul_f32 v[122:123], v[122:123], v[168:169] op_sel_hi:[1,0]
	v_pk_mul_f32 v[116:117], v[116:117], v[178:179] op_sel_hi:[1,0]
	v_pk_mul_f32 v[118:119], v[118:119], v[168:169] op_sel_hi:[1,0]
	v_pk_mul_f32 v[70:71], v[70:71], v[178:179] op_sel_hi:[1,0]
	v_pk_mul_f32 v[72:73], v[72:73], v[168:169] op_sel_hi:[1,0]
	v_pk_mul_f32 v[66:67], v[66:67], v[178:179] op_sel_hi:[1,0]
	v_pk_mul_f32 v[68:69], v[68:69], v[168:169] op_sel_hi:[1,0]
	s_waitcnt vmcnt(2)
	v_pk_add_f32 v[160:161], v[160:161], 1.0 op_sel_hi:[1,0]
	s_waitcnt vmcnt(1)
	v_pk_mul_f32 v[160:161], v[190:191], v[160:161]
	v_pk_add_f32 v[162:163], v[162:163], 1.0 op_sel_hi:[1,0]
	s_waitcnt vmcnt(0)
	v_pk_fma_f32 v[152:153], v[152:153], v[160:161], v[210:211]
	v_pk_mul_f32 v[162:163], v[192:193], v[162:163]
	v_pk_fma_f32 v[156:157], v[156:157], v[160:161], v[210:211]
	v_cvt_pk_bf16_f32 v160, v152, v153
	v_med3_f32 v152, v152, s68, v203
	v_med3_f32 v153, v153, s68, v203
	v_pk_fma_f32 v[150:151], v[150:151], v[162:163], v[212:213]
	v_pk_fma_f32 v[154:155], v[154:155], v[162:163], v[212:213]
	v_med3_f32 v162, v156, s68, v203
	v_cvt_pk_fp8_f32 v159, v152, v153
	v_med3_f32 v152, v157, s68, v203
	v_cvt_pk_fp8_f32 v207, v162, v152
	v_cvt_pk_bf16_f32 v161, v150, v151
	v_med3_f32 v150, v150, s68, v203
	v_med3_f32 v151, v151, s68, v203
	v_med3_f32 v153, v154, s68, v203
	v_cvt_pk_fp8_f32 v159, v150, v151 op_sel:[0,0,1]
	v_med3_f32 v150, v155, s68, v203
	v_cvt_pk_fp8_f32 v207, v153, v150 op_sel:[0,0,1]
	ds_write_b64 v187, v[160:161] offset:512
	global_store_dword v[142:143], v159, off offset:256
	v_cvt_pk_bf16_f32 v164, v156, v157
	v_cvt_pk_bf16_f32 v165, v154, v155
	global_store_dword v[166:167], v207, off offset:256
	global_load_dwordx4 v[150:153], v[184:185], off offset:2048
	global_load_dwordx4 v[154:157], v[188:189], off offset:2048
	global_load_dwordx4 v[160:163], v[180:181], off offset:2048
	v_mov_b32_e32 v159, 0
	ds_write_b64 v158, v[164:165] offset:512
	v_mov_b32_e32 v190, 0
	s_waitcnt vmcnt(2)
	v_pk_add_f32 v[150:151], v[150:151], 1.0 op_sel_hi:[1,0]
	s_waitcnt vmcnt(1)
	v_pk_mul_f32 v[150:151], v[154:155], v[150:151]
	v_pk_add_f32 v[152:153], v[152:153], 1.0 op_sel_hi:[1,0]
	s_waitcnt vmcnt(0)
	v_pk_fma_f32 v[144:145], v[144:145], v[150:151], v[160:161]
	v_pk_mul_f32 v[152:153], v[156:157], v[152:153]
	v_pk_fma_f32 v[148:149], v[148:149], v[150:151], v[160:161]
	v_cvt_pk_bf16_f32 v150, v144, v145
	v_med3_f32 v144, v144, s68, v203
	v_med3_f32 v145, v145, s68, v203
	v_pk_fma_f32 v[140:141], v[140:141], v[152:153], v[162:163]
	v_pk_fma_f32 v[146:147], v[146:147], v[152:153], v[162:163]
	v_med3_f32 v152, v148, s68, v203
	v_cvt_pk_fp8_f32 v159, v144, v145
	v_med3_f32 v144, v149, s68, v203
	v_cvt_pk_fp8_f32 v190, v152, v144
	v_cvt_pk_bf16_f32 v151, v140, v141
	v_med3_f32 v140, v140, s68, v203
	v_med3_f32 v141, v141, s68, v203
	v_med3_f32 v145, v146, s68, v203
	v_cvt_pk_fp8_f32 v159, v140, v141 op_sel:[0,0,1]
	v_med3_f32 v140, v147, s68, v203
	v_cvt_pk_fp8_f32 v190, v145, v140 op_sel:[0,0,1]
	ds_write_b64 v187, v[150:151] offset:1024
	global_store_dword v[142:143], v159, off offset:512
	v_cvt_pk_bf16_f32 v160, v148, v149
	v_cvt_pk_bf16_f32 v161, v146, v147
	global_store_dword v[166:167], v190, off offset:512
	global_load_dwordx4 v[146:149], v[184:185], off offset:3072
	global_load_dwordx4 v[150:153], v[188:189], off offset:3072
	global_load_dwordx4 v[154:157], v[180:181], off offset:3072
	v_mov_b32_e32 v159, 0
	ds_write_b64 v158, v[160:161] offset:1024
	v_mov_b32_e32 v162, 0
	v_add_co_u32_e32 v140, vcc, s69, v188
	s_waitcnt vmcnt(2)
	v_pk_add_f32 v[146:147], v[146:147], 1.0 op_sel_hi:[1,0]
	s_waitcnt vmcnt(1)
	v_pk_mul_f32 v[146:147], v[150:151], v[146:147]
	v_pk_add_f32 v[148:149], v[148:149], 1.0 op_sel_hi:[1,0]
	s_waitcnt vmcnt(0)
	v_pk_fma_f32 v[136:137], v[136:137], v[146:147], v[154:155]
	v_pk_mul_f32 v[148:149], v[152:153], v[148:149]
	v_pk_fma_f32 v[138:139], v[138:139], v[146:147], v[154:155]
	v_cvt_pk_bf16_f32 v146, v136, v137
	v_med3_f32 v136, v136, s68, v203
	v_med3_f32 v137, v137, s68, v203
	v_pk_fma_f32 v[132:133], v[132:133], v[148:149], v[156:157]
	v_pk_fma_f32 v[134:135], v[134:135], v[148:149], v[156:157]
	v_med3_f32 v148, v138, s68, v203
	v_cvt_pk_fp8_f32 v159, v136, v137
	v_med3_f32 v136, v139, s68, v203
	v_cvt_pk_fp8_f32 v162, v148, v136
	v_cvt_pk_bf16_f32 v147, v132, v133
	v_med3_f32 v132, v132, s68, v203
	v_med3_f32 v133, v133, s68, v203
	v_med3_f32 v137, v134, s68, v203
	v_cvt_pk_fp8_f32 v159, v132, v133 op_sel:[0,0,1]
	v_med3_f32 v132, v135, s68, v203
	v_cvt_pk_fp8_f32 v162, v137, v132 op_sel:[0,0,1]
	v_addc_co_u32_e32 v141, vcc, 0, v189, vcc
	v_add_co_u32_e32 v144, vcc, s69, v184
	ds_write_b64 v187, v[146:147] offset:1536
	s_nop 0
	v_addc_co_u32_e32 v145, vcc, 0, v185, vcc
	global_store_dword v[142:143], v159, off offset:768
	v_cvt_pk_bf16_f32 v138, v138, v139
	v_cvt_pk_bf16_f32 v139, v134, v135
	global_store_dword v[166:167], v162, off offset:768
	global_load_dwordx4 v[134:137], v[140:141], off
	global_load_dwordx4 v[146:149], v[144:145], off
	v_add_co_u32_e32 v132, vcc, s69, v180
	ds_write_b64 v158, v[138:139] offset:1536
	s_nop 0
	v_addc_co_u32_e32 v133, vcc, 0, v181, vcc
	global_load_dwordx4 v[150:153], v[132:133], off
	v_mov_b32_e32 v154, 0
	v_mov_b32_e32 v155, 0
	s_and_b64 vcc, exec, s[56:57]
	s_waitcnt vmcnt(1)
	v_pk_add_f32 v[146:147], v[146:147], 1.0 op_sel_hi:[1,0]
	s_nop 0
	v_pk_mul_f32 v[134:135], v[134:135], v[146:147]
	v_pk_add_f32 v[138:139], v[148:149], 1.0 op_sel_hi:[1,0]
	v_mov_b32_e32 v146, 0
	v_pk_mul_f32 v[136:137], v[136:137], v[138:139]
	v_mov_b32_e32 v147, 0
	s_waitcnt vmcnt(0)
	v_pk_fma_f32 v[128:129], v[128:129], v[134:135], v[150:151]
	v_pk_fma_f32 v[130:131], v[130:131], v[134:135], v[150:151]
	v_cvt_pk_bf16_f32 v134, v128, v129
	v_med3_f32 v128, v128, s68, v203
	v_med3_f32 v129, v129, s68, v203
	v_pk_fma_f32 v[124:125], v[124:125], v[136:137], v[152:153]
	v_pk_fma_f32 v[126:127], v[126:127], v[136:137], v[152:153]
	v_med3_f32 v136, v130, s68, v203
	v_cvt_pk_fp8_f32 v154, v128, v129
	v_med3_f32 v128, v131, s68, v203
	v_cvt_pk_fp8_f32 v155, v136, v128
	v_cvt_pk_bf16_f32 v135, v124, v125
	v_med3_f32 v124, v124, s68, v203
	v_med3_f32 v125, v125, s68, v203
	v_med3_f32 v129, v126, s68, v203
	v_cvt_pk_fp8_f32 v154, v124, v125 op_sel:[0,0,1]
	v_med3_f32 v124, v127, s68, v203
	v_cvt_pk_fp8_f32 v155, v129, v124 op_sel:[0,0,1]
	ds_write_b64 v187, v[134:135] offset:2048
	global_store_dword v[142:143], v154, off offset:1024
	v_cvt_pk_bf16_f32 v138, v130, v131
	v_cvt_pk_bf16_f32 v139, v126, v127
	global_store_dword v[166:167], v155, off offset:1024
	global_load_dwordx4 v[124:127], v[144:145], off offset:1024
	global_load_dwordx4 v[128:131], v[140:141], off offset:1024
	global_load_dwordx4 v[134:137], v[132:133], off offset:1024
	ds_write_b64 v158, v[138:139] offset:2048
	s_waitcnt vmcnt(2)
	v_pk_add_f32 v[124:125], v[124:125], 1.0 op_sel_hi:[1,0]
	s_waitcnt vmcnt(1)
	v_pk_mul_f32 v[124:125], v[128:129], v[124:125]
	v_pk_add_f32 v[126:127], v[126:127], 1.0 op_sel_hi:[1,0]
	s_waitcnt vmcnt(0)
	v_pk_fma_f32 v[120:121], v[120:121], v[124:125], v[134:135]
	v_pk_mul_f32 v[126:127], v[130:131], v[126:127]
	v_pk_fma_f32 v[122:123], v[122:123], v[124:125], v[134:135]
	v_cvt_pk_bf16_f32 v124, v120, v121
	v_med3_f32 v120, v120, s68, v203
	v_med3_f32 v121, v121, s68, v203
	v_pk_fma_f32 v[116:117], v[116:117], v[126:127], v[136:137]
	v_pk_fma_f32 v[118:119], v[118:119], v[126:127], v[136:137]
	v_med3_f32 v126, v122, s68, v203
	v_cvt_pk_fp8_f32 v146, v120, v121
	v_med3_f32 v120, v123, s68, v203
	v_cvt_pk_fp8_f32 v147, v126, v120
	v_cvt_pk_bf16_f32 v125, v116, v117
	v_med3_f32 v116, v116, s68, v203
	v_med3_f32 v117, v117, s68, v203
	v_med3_f32 v121, v118, s68, v203
	v_cvt_pk_fp8_f32 v146, v116, v117 op_sel:[0,0,1]
	v_med3_f32 v116, v119, s68, v203
	v_cvt_pk_fp8_f32 v147, v121, v116 op_sel:[0,0,1]
	ds_write_b64 v187, v[124:125] offset:2560
	global_store_dword v[142:143], v146, off offset:1280
	v_cvt_pk_bf16_f32 v128, v122, v123
	v_cvt_pk_bf16_f32 v129, v118, v119
	global_store_dword v[166:167], v147, off offset:1280
	global_load_dwordx4 v[116:119], v[144:145], off offset:2048
	global_load_dwordx4 v[120:123], v[140:141], off offset:2048
	global_load_dwordx4 v[124:127], v[132:133], off offset:2048
	v_pk_mul_f32 v[130:131], v[174:175], v[178:179] op_sel_hi:[1,0]
	v_pk_mul_f32 v[134:135], v[176:177], v[168:169] op_sel_hi:[1,0]
	v_mov_b32_e32 v136, 0
	ds_write_b64 v158, v[128:129] offset:2560
	v_mov_b32_e32 v137, 0
	v_pk_mul_f32 v[128:129], v[172:173], v[168:169] op_sel_hi:[1,0]
	s_waitcnt vmcnt(2)
	v_pk_add_f32 v[116:117], v[116:117], 1.0 op_sel_hi:[1,0]
	v_pk_add_f32 v[118:119], v[118:119], 1.0 op_sel_hi:[1,0]
	s_waitcnt vmcnt(1)
	v_pk_mul_f32 v[116:117], v[120:121], v[116:117]
	v_pk_mul_f32 v[118:119], v[122:123], v[118:119]
	s_waitcnt vmcnt(0)
	v_pk_fma_f32 v[120:121], v[130:131], v[116:117], v[124:125]
	v_pk_fma_f32 v[70:71], v[70:71], v[118:119], v[126:127]
	v_pk_fma_f32 v[72:73], v[72:73], v[118:119], v[126:127]
	v_pk_fma_f32 v[116:117], v[134:135], v[116:117], v[124:125]
	v_cvt_pk_bf16_f32 v118, v120, v121
	v_med3_f32 v120, v120, s68, v203
	v_med3_f32 v121, v121, s68, v203
	v_med3_f32 v122, v116, s68, v203
	v_cvt_pk_fp8_f32 v136, v120, v121
	v_med3_f32 v120, v117, s68, v203
	v_cvt_pk_fp8_f32 v137, v122, v120
	v_cvt_pk_bf16_f32 v119, v70, v71
	v_med3_f32 v70, v70, s68, v203
	v_med3_f32 v71, v71, s68, v203
	v_med3_f32 v121, v72, s68, v203
	v_cvt_pk_fp8_f32 v136, v70, v71 op_sel:[0,0,1]
	v_med3_f32 v70, v73, s68, v203
	v_cvt_pk_fp8_f32 v137, v121, v70 op_sel:[0,0,1]
	ds_write_b64 v187, v[118:119] offset:3072
	global_store_dword v[142:143], v136, off offset:1536
	v_cvt_pk_bf16_f32 v124, v116, v117
	v_cvt_pk_bf16_f32 v125, v72, v73
	global_store_dword v[166:167], v137, off offset:1536
	global_load_dwordx4 v[70:73], v[144:145], off offset:3072
	global_load_dwordx4 v[116:119], v[140:141], off offset:3072
	global_load_dwordx4 v[120:123], v[132:133], off offset:3072
	v_pk_mul_f32 v[126:127], v[170:171], v[178:179] op_sel_hi:[1,0]
	v_mov_b32_e32 v130, 0
	ds_write_b64 v158, v[124:125] offset:3072
	v_mov_b32_e32 v131, 0
	s_waitcnt vmcnt(2)
	v_pk_add_f32 v[70:71], v[70:71], 1.0 op_sel_hi:[1,0]
	v_pk_add_f32 v[72:73], v[72:73], 1.0 op_sel_hi:[1,0]
	s_waitcnt vmcnt(1)
	v_pk_mul_f32 v[70:71], v[116:117], v[70:71]
	v_pk_mul_f32 v[72:73], v[118:119], v[72:73]
	s_waitcnt vmcnt(0)
	v_pk_fma_f32 v[116:117], v[126:127], v[70:71], v[120:121]
	v_pk_fma_f32 v[66:67], v[66:67], v[72:73], v[122:123]
	v_pk_fma_f32 v[68:69], v[68:69], v[72:73], v[122:123]
	v_pk_fma_f32 v[70:71], v[128:129], v[70:71], v[120:121]
	v_cvt_pk_bf16_f32 v72, v116, v117
	v_med3_f32 v116, v116, s68, v203
	v_med3_f32 v117, v117, s68, v203
	v_med3_f32 v118, v70, s68, v203
	v_cvt_pk_fp8_f32 v130, v116, v117
	v_med3_f32 v116, v71, s68, v203
	v_cvt_pk_fp8_f32 v131, v118, v116
	v_cvt_pk_bf16_f32 v73, v66, v67
	v_med3_f32 v66, v66, s68, v203
	v_med3_f32 v67, v67, s68, v203
	v_med3_f32 v117, v68, s68, v203
	v_cvt_pk_fp8_f32 v130, v66, v67 op_sel:[0,0,1]
	v_med3_f32 v66, v69, s68, v203
	v_cvt_pk_fp8_f32 v131, v117, v66 op_sel:[0,0,1]
	ds_write_b64 v187, v[72:73] offset:3584
	global_store_dword v[142:143], v130, off offset:1792
	v_cvt_pk_bf16_f32 v66, v70, v71
	v_cvt_pk_bf16_f32 v67, v68, v69
	global_store_dword v[166:167], v131, off offset:1792
	ds_write_b64 v158, v[66:67] offset:3584
	s_waitcnt lgkmcnt(0)
	s_barrier
	s_cbranch_vccnz .LBB0_1139
	s_add_i32 s16, s73, s62
	s_ashr_i32 s17, s16, 31
	s_or_b32 s18, s16, 1
	s_lshl_b64 s[20:21], s[16:17], 13
	v_readlane_b32 s76, v252, 9
	v_readlane_b32 s77, v252, 10
	s_add_u32 s20, s76, s20
	s_addc_u32 s21, s77, s21
	s_ashr_i32 s19, s18, 31
	s_lshl_b64 s[22:23], s[18:19], 13
	s_add_u32 s22, s76, s22
	s_addc_u32 s23, s77, s23
	s_lshl_b64 s[16:17], s[16:17], 12
	v_lshl_add_u64 v[66:67], v[100:101], 0, s[16:17]
	s_lshl_b64 s[16:17], s[18:19], 12
	v_lshl_add_u64 v[68:69], v[100:101], 0, s[16:17]
	global_load_dwordx4 v[2:5], v195, s[20:21]
	global_load_dwordx4 v[6:9], v195, s[20:21] offset:1024
	global_load_dwordx4 v[10:13], v195, s[22:23]
	global_load_dwordx4 v[14:17], v195, s[22:23] offset:1024
	global_load_dwordx4 v[18:21], v195, s[20:21] offset:2048
	global_load_dwordx4 v[22:25], v195, s[20:21] offset:3072
	global_load_dwordx4 v[26:29], v195, s[22:23] offset:2048
	global_load_dwordx4 v[30:33], v195, s[22:23] offset:3072
	global_load_dwordx2 v[74:75], v[66:67], off
	global_load_dwordx2 v[76:77], v[66:67], off offset:512
	global_load_dwordx2 v[78:79], v[66:67], off offset:1024
	global_load_dwordx2 v[80:81], v[66:67], off offset:1536
	global_load_dwordx2 v[82:83], v[68:69], off
	global_load_dwordx2 v[84:85], v[68:69], off offset:512
	global_load_dwordx2 v[88:89], v[68:69], off offset:1024
	global_load_dwordx2 v[90:91], v[68:69], off offset:1536
	global_load_dwordx4 v[34:37], v196, s[20:21]
	global_load_dwordx4 v[38:41], v196, s[22:23]
	global_load_dwordx4 v[42:45], v197, s[20:21]
	global_load_dwordx4 v[46:49], v197, s[22:23]
	global_load_dwordx4 v[50:53], v198, s[20:21]
	global_load_dwordx4 v[54:57], v198, s[22:23]
	global_load_dwordx4 v[58:61], v199, s[20:21]
	global_load_dwordx4 v[62:65], v199, s[22:23]
	global_load_dwordx2 v[94:95], v[66:67], off offset:2048
	global_load_dwordx2 v[96:97], v[66:67], off offset:2560
	global_load_dwordx2 v[98:99], v[66:67], off offset:3072
	global_load_dwordx2 v[102:103], v[66:67], off offset:3584
	global_load_dwordx2 v[104:105], v[68:69], off offset:2048
	global_load_dwordx2 v[106:107], v[68:69], off offset:2560
	global_load_dwordx2 v[108:109], v[68:69], off offset:3072
	global_load_dwordx2 v[110:111], v[68:69], off offset:3584
	v_readlane_b32 s78, v252, 11
	v_readlane_b32 s79, v252, 12
	v_readlane_b32 s80, v252, 13
	v_readlane_b32 s81, v252, 14
	v_readlane_b32 s82, v252, 15
	v_readlane_b32 s83, v252, 16
	v_readlane_b32 s84, v252, 17
	v_readlane_b32 s85, v252, 18
	v_readlane_b32 s86, v252, 19
	v_readlane_b32 s87, v252, 20
	v_readlane_b32 s88, v252, 21
	v_readlane_b32 s89, v252, 22
	v_readlane_b32 s90, v252, 23
	v_readlane_b32 s91, v252, 24
